# split v_pk_add_f32 into scalar adds in attention inner loops
# speedup vs baseline: 1.0097x; 1.0097x over previous
; #define ATT_SBAR() __builtin_amdgcn_sched_barrier(0)
;     __device__ __forceinline__ void init(f32x16& c0, f32x16& c1, int t) const {
;         float base = slope2 * ((float)(64 * t + 4 * hi) - tqf);
;         if (t < nb0) { if (!((selmask >> (t >> 2)) & 1u)) base = ATT_NEG; }
;         const float d32 = 32.0f * slope2;
; #pragma unroll
;         for (int i = 0; i < 8; ++i) { const int r = 2 * i; const f32x2_t kc = (f32x2_t){slope2 * (float)((r & 3) + 8 * (r >> 2)), slope2 * (float)(((r + 1) & 3) + 8 * ((r + 1) >> 2))};
;             const f32x2_t p = kc + base, q = p + d32; c0[r] = p[0]; c0[r + 1] = p[1]; c1[r] = q[0]; c1[r + 1] = q[1]; }
;         if (t - nb0 == (w >> 1)) {
; #pragma unroll
;             for (int r = 0; r < 16; ++r) { const int ko = (r & 3) + 8 * (r >> 2); if (ko > u) c0[r] = ATT_NEG; if (ko > u - 32) c1[r] = ATT_NEG; }
;         }
;     }
; template <class BIAS>
; __device__ __forceinline__ void attn_tiles(char* shm, const UnitIO& io, int t_begin, int t_end, const BIAS& B, int tid) {
;     ...
;         u32x4 pw[4]; f32x16 c1x;
;         if (act) {
;             bf16x8 kf[8]; const lds_cptr kp = kp0 + sl_c;
; #pragma unroll
;             for (int j = 0; j < 4; ++j) { kf[2 * j] = *(const __attribute__((address_space(3))) bf16x8*)(kp + j * 2048); kf[2 * j + 1] = *(const __attribute__((address_space(3))) bf16x8*)(kp + j * 2048 + 512); }
;             ATT_SBAR();
;             f32x16 c0, c1; B.init(c0, c1, t);
;             ATT_SBAR();
;             asm volatile("" : "+v"(kf[0]), "+v"(kf[1]), "+v"(kf[2]), "+v"(kf[3]), "+v"(kf[4]), "+v"(kf[5]), "+v"(kf[6]), "+v"(kf[7]));
; #pragma unroll
;             for (int d0 = 0; d0 < 4; ++d0) { c0 = __builtin_amdgcn_mfma_f32_32x32x16_bf16(kf[2 * d0], qr[d0], c0, 0, 0, 0); c1 = __builtin_amdgcn_mfma_f32_32x32x16_bf16(kf[2 * d0 + 1], qr[d0], c1, 0, 0, 0); }
;             float s0 = 0.f;
; #pragma unroll
;             for (int r = 0; r < 16; ++r) c0[r] = __builtin_amdgcn_exp2f(c0[r]);
;             { f32x2_t s2 = (f32x2_t){c0[0], c0[1]};
; #pragma unroll
;               for (int i = 1; i < 8; ++i) s2 += (f32x2_t){c0[2 * i], c0[2 * i + 1]};
;               s0 = s2[0] + s2[1]; }
;             l_reg += s0;
; #pragma unroll
;             for (int i = 0; i < 4; ++i) { pw[0][i] = cvtpk(c0[2 * i], c0[2 * i + 1]); pw[1][i] = cvtpk(c0[8 + 2 * i], c0[9 + 2 * i]); }
;             c1x = c1;
.LBB0_298:
	s_add_i32 s34, s20, s17
	s_cmp_lt_u32 s17, s26
	s_cselect_b64 s[14:15], -1, 0
	s_cmp_le_i32 s34, s73
	s_cselect_b64 s[4:5], -1, 0
	s_or_b64 vcc, s[14:15], s[4:5]
	s_add_i32 s4, s22, 0xffffa000
	v_cndmask_b32_e64 v58, 0, 1, vcc
	s_and_b32 s23, s4, 0x6000
	v_cmp_ne_u32_e64 s[4:5], 1, v58
	s_andn2_b64 vcc, exec, vcc
	s_cbranch_vccnz .LBB0_310
	v_add_u32_e32 v34, s23, v181
	ds_read_b128 v[98:101], v34
	ds_read_b128 v[94:97], v34 offset:512
	ds_read_b128 v[102:105], v34 offset:2048
	ds_read_b128 v[90:93], v34 offset:2560
	ds_read_b128 v[106:109], v34 offset:4096
	ds_read_b128 v[86:89], v34 offset:4608
	ds_read_b128 v[110:113], v34 offset:6144
	ds_read_b128 v[82:85], v34 offset:6656
	s_add_i32 s35, s24, s17
	v_cvt_f32_u32_e32 v34, v149
	s_lshr_b32 vcc_lo, s17, 2
	s_lshl_b32 vcc_lo, 1, vcc_lo
	v_and_b32_e32 v35, vcc_lo, v135
	v_sub_f32_e32 v34, v34, v137
	v_cmp_eq_u32_e32 vcc, 0, v35
	v_mul_f32_e32 v34, v115, v34
	s_and_b64 vcc, s[14:15], vcc
	v_cndmask_b32_e32 v34, v34, v226, vcc
	v_add_f32_e32 v50, v114, v34
	v_add_f32_e32 v51, v115, v34
	v_add_f32_e32 v52, v118, v34
	v_add_f32_e32 v53, v119, v34
	v_add_f32_e32 v54, v120, v34
	v_add_f32_e32 v55, v121, v34
	v_add_f32_e32 v56, v122, v34
	v_add_f32_e32 v57, v123, v34
	v_add_f32_e32 v58, v124, v34
	v_add_f32_e32 v59, v125, v34
	v_add_f32_e32 v60, v126, v34
	v_add_f32_e32 v61, v127, v34
	v_add_f32_e32 v62, v128, v34
	v_add_f32_e32 v63, v129, v34
	v_add_f32_e32 v64, v140, v34
	v_add_f32_e32 v65, v141, v34
	v_mov_b32_e32 v117, v116
	v_add_f32_e32 v48, v116, v64
	v_add_f32_e32 v49, v117, v65
	v_add_f32_e32 v46, v116, v62
	v_add_f32_e32 v47, v117, v63
	v_add_f32_e32 v44, v116, v60
	v_add_f32_e32 v45, v117, v61
	v_add_f32_e32 v42, v116, v58
	v_add_f32_e32 v43, v117, v59
	v_add_f32_e32 v40, v116, v56
	v_add_f32_e32 v41, v117, v57
	v_add_f32_e32 v38, v116, v54
	v_add_f32_e32 v39, v117, v55
	v_add_f32_e32 v36, v116, v52
	v_add_f32_e32 v37, v117, v53
	s_cmp_lg_u32 s35, 0
	v_add_f32_e32 v34, v162, v50
	v_add_f32_e32 v35, v163, v51
	s_cbranch_scc1 .LBB0_303
	v_cndmask_b32_e64 v48, v48, v226, s[36:37]
	v_cndmask_b32_e64 v47, v47, v226, s[40:41]
	v_cndmask_b32_e64 v46, v46, v226, s[42:43]
	v_cndmask_b32_e64 v45, v45, v226, s[44:45]
	v_cndmask_b32_e64 v44, v44, v226, s[46:47]
	v_cndmask_b32_e64 v43, v43, v226, s[48:49]
	v_cndmask_b32_e64 v42, v42, v226, s[50:51]
	v_cndmask_b32_e64 v41, v41, v226, s[52:53]
	v_cndmask_b32_e64 v40, v40, v226, s[54:55]
	v_cndmask_b32_e64 v39, v39, v226, s[56:57]
	v_cndmask_b32_e64 v38, v38, v226, s[58:59]
	v_cndmask_b32_e64 v37, v37, v226, s[60:61]
	v_cndmask_b32_e64 v36, v36, v226, s[62:63]
	v_cndmask_b32_e64 v35, v35, v226, s[64:65]
	v_cndmask_b32_e64 v34, v34, v226, s[66:67]
	s_and_saveexec_b64 s[14:15], s[6:7]
	s_mov_b32 s35, 0xff800000
	v_mov_b32_e32 v49, s35
	s_or_b64 exec, exec, s[14:15]
	v_cndmask_b32_e64 v65, v65, v226, s[38:39]
	v_cndmask_b32_e64 v50, v50, v226, s[96:97]
	v_cndmask_b32_e64 v51, v51, v226, s[94:95]
	v_cndmask_b32_e64 v52, v52, v226, s[92:93]
	v_cndmask_b32_e64 v53, v53, v226, s[90:91]
	v_cndmask_b32_e64 v54, v54, v226, s[88:89]
	v_cndmask_b32_e64 v55, v55, v226, s[2:3]
	v_cndmask_b32_e64 v56, v56, v226, s[84:85]
	v_cndmask_b32_e64 v57, v57, v226, s[82:83]
	v_cndmask_b32_e64 v58, v58, v226, s[80:81]
	v_cndmask_b32_e64 v59, v59, v226, s[78:79]
	v_cndmask_b32_e64 v60, v60, v226, s[76:77]
	v_cndmask_b32_e64 v61, v61, v226, s[74:75]
	v_cndmask_b32_e64 v62, v62, v226, s[18:19]
	v_cndmask_b32_e64 v63, v63, v226, s[70:71]
	v_cndmask_b32_e64 v64, v64, v226, s[68:69]
.LBB0_303:
	s_waitcnt lgkmcnt(0)
	s_nop 0
	v_mfma_f32_32x32x16_bf16 v[50:65], v[98:101], v[66:69], v[50:65]
	v_mfma_f32_32x32x16_bf16 v[50:65], v[102:105], v[70:73], v[50:65]
	v_mfma_f32_32x32x16_bf16 v[34:49], v[94:97], v[66:69], v[34:49]
	v_mfma_f32_32x32x16_bf16 v[50:65], v[106:109], v[74:77], v[50:65]
	v_mfma_f32_32x32x16_bf16 v[34:49], v[90:93], v[70:73], v[34:49]
	v_mfma_f32_32x32x16_bf16 v[50:65], v[110:113], v[78:81], v[50:65]
	v_mfma_f32_32x32x16_bf16 v[34:49], v[86:89], v[74:77], v[34:49]
	s_nop 10
	v_exp_f32_e32 v50, v50
	v_exp_f32_e32 v51, v51
	v_exp_f32_e32 v52, v52
	v_exp_f32_e32 v53, v53
	v_exp_f32_e32 v98, v54
	v_exp_f32_e32 v99, v55
	v_exp_f32_e32 v100, v56
	v_exp_f32_e32 v101, v57
	v_exp_f32_e32 v54, v58
	v_exp_f32_e32 v55, v59
	v_exp_f32_e32 v56, v60
	v_exp_f32_e32 v57, v61
	v_exp_f32_e32 v58, v62
	v_exp_f32_e32 v59, v63
	v_add_f32_e32 v62, v50, v52
	v_add_f32_e32 v63, v51, v53
	v_mfma_f32_32x32x16_bf16 v[34:49], v[82:85], v[78:81], v[34:49]
	v_add_f32_e64 v62, v98, v62
	v_add_f32_e64 v63, v99, v63
	v_exp_f32_e32 v60, v64
	v_exp_f32_e32 v61, v65
	v_add_f32_e32 v62, v100, v62
	v_add_f32_e32 v63, v101, v63
	v_cvt_pk_bf16_f32 v50, v50, v51
	v_add_f32_e32 v62, v54, v62
	v_add_f32_e32 v63, v55, v63
	v_cvt_pk_bf16_f32 v54, v54, v55
	v_add_f32_e32 v62, v56, v62
	v_add_f32_e32 v63, v57, v63
	v_cvt_pk_bf16_f32 v51, v52, v53
	v_add_f32_e32 v62, v58, v62
	v_add_f32_e32 v63, v59, v63
	v_cvt_pk_bf16_f32 v55, v56, v57
	v_add_f32_e32 v62, v60, v62
	v_add_f32_e32 v63, v61, v63
	v_cvt_pk_bf16_f32 v52, v98, v99
	v_add_f32_e32 v62, v62, v63
	v_cvt_pk_bf16_f32 v56, v58, v59
	v_cvt_pk_bf16_f32 v53, v100, v101
	v_cvt_pk_bf16_f32 v57, v60, v61
	v_add_f32_e32 v139, v139, v62
	s_and_b64 vcc, exec, s[4:5]
	s_cbranch_vccz .LBB0_311

; __device__ __forceinline__ unsigned cvtpk(float lo, float hi) { f32x2_t v = {lo, hi}; bf16x2_t b = __builtin_convertvector(v, bf16x2_t); return __builtin_bit_cast(unsigned, b); }
; __device__ __forceinline__ s16x4 vtr(lds_cptr p) { return __builtin_bit_cast(s16x4, __builtin_amdgcn_ds_read_tr16_b64_v4i16((__attribute__((address_space(3))) v4i16_t*)p)); }
; template <class BIAS>
; __device__ __forceinline__ void attn_tiles(char* shm, const UnitIO& io, int t_begin, int t_end, const BIAS& B, int tid) {
;     ...
;         if (act) {
;             const lds_cptr vp = vp0 + sl_c;
;             s16x4 vlo[8], vhi[8];
; #pragma unroll
;             for (int i = 0; i < 8; ++i) { vlo[i] = vtr(vp + (i >> 2) * 4096 + (i & 3) * 1024); vhi[i] = vtr(vp + (i >> 2) * 4096 + (i & 3) * 1024 + 512); }
;             ATT_SBAR();
;             { float s1 = 0.f;
; #pragma unroll
;               for (int r = 0; r < 16; ++r) c1x[r] = __builtin_amdgcn_exp2f(c1x[r]);
;               { f32x2_t s2 = (f32x2_t){c1x[0], c1x[1]};
; #pragma unroll
;                 for (int i = 1; i < 8; ++i) s2 += (f32x2_t){c1x[2 * i], c1x[2 * i + 1]};
;                 s1 = s2[0] + s2[1]; }
;               l_reg += s1;
; #pragma unroll
;               for (int i = 0; i < 4; ++i) { pw[2][i] = cvtpk(c1x[2 * i], c1x[2 * i + 1]); pw[3][i] = cvtpk(c1x[8 + 2 * i], c1x[9 + 2 * i]); } }
;             ATT_SBAR();
;             asm volatile("" : "+v"(vlo[0]), "+v"(vhi[0]), "+v"(vlo[1]), "+v"(vhi[1]), "+v"(vlo[2]), "+v"(vhi[2]), "+v"(vlo[3]), "+v"(vhi[3]));
; #pragma unroll
;             for (int ks = 0; ks < 4; ++ks) { const bf16x8 vf = (bf16x8){vlo[ks][0], vlo[ks][1], vlo[ks][2], vlo[ks][3], vhi[ks][0], vhi[ks][1], vhi[ks][2], vhi[ks][3]};
;                 o[0] = __builtin_amdgcn_mfma_f32_32x32x16_bf16(__builtin_bit_cast(bf16x8, pw[ks]), vf, o[0], 0, 0, 0); }
;             ATT_SBAR();
;             asm volatile("" : "+v"(vlo[4]), "+v"(vhi[4]), "+v"(vlo[5]), "+v"(vhi[5]), "+v"(vlo[6]), "+v"(vhi[6]), "+v"(vlo[7]), "+v"(vhi[7]));
; #pragma unroll
;             for (int ks = 0; ks < 4; ++ks) { const bf16x8 vf = (bf16x8){vlo[4 + ks][0], vlo[4 + ks][1], vlo[4 + ks][2], vlo[4 + ks][3], vhi[4 + ks][0], vhi[4 + ks][1], vhi[4 + ks][2], vhi[4 + ks][3]};
;                 o[1] = __builtin_amdgcn_mfma_f32_32x32x16_bf16(__builtin_bit_cast(bf16x8, pw[ks]), vf, o[1], 0, 0, 0); }
;         }
.LBB0_311:
	v_add_u32_e32 v104, s23, v180
	ds_read_b64_tr_b16 v[58:59], v104 offset:32768
	ds_read_b64_tr_b16 v[60:61], v104 offset:33280
	ds_read_b64_tr_b16 v[62:63], v104 offset:33792
	ds_read_b64_tr_b16 v[64:65], v104 offset:34304
	ds_read_b64_tr_b16 v[82:83], v104 offset:34816
	ds_read_b64_tr_b16 v[84:85], v104 offset:35328
	ds_read_b64_tr_b16 v[86:87], v104 offset:35840
	ds_read_b64_tr_b16 v[88:89], v104 offset:36352
	ds_read_b64_tr_b16 v[90:91], v104 offset:36864
	ds_read_b64_tr_b16 v[92:93], v104 offset:37376
	ds_read_b64_tr_b16 v[94:95], v104 offset:37888
	ds_read_b64_tr_b16 v[96:97], v104 offset:38400
	ds_read_b64_tr_b16 v[98:99], v104 offset:38912
	ds_read_b64_tr_b16 v[100:101], v104 offset:39424
	ds_read_b64_tr_b16 v[102:103], v104 offset:39936
	ds_read_b64_tr_b16 v[104:105], v104 offset:40448
	v_exp_f32_e32 v34, v34
	v_exp_f32_e32 v35, v35
	v_exp_f32_e32 v36, v36
	v_exp_f32_e32 v37, v37
	v_exp_f32_e32 v38, v38
	v_exp_f32_e32 v39, v39
	v_exp_f32_e32 v40, v40
	v_exp_f32_e32 v41, v41
	v_exp_f32_e32 v42, v42
	v_exp_f32_e32 v43, v43
	v_exp_f32_e32 v44, v44
	v_exp_f32_e32 v45, v45
	v_add_f32_e32 v106, v36, v34
	v_add_f32_e32 v107, v37, v35
	v_exp_f32_e32 v46, v46
	v_exp_f32_e32 v47, v47
	v_add_f32_e32 v106, v38, v106
	v_add_f32_e32 v107, v39, v107
	v_exp_f32_e32 v48, v48
	v_exp_f32_e32 v49, v49
	v_add_f32_e32 v106, v40, v106
	v_add_f32_e32 v107, v41, v107
	v_cvt_pk_bf16_f32 v110, v42, v43
	v_add_f32_e32 v106, v42, v106
	v_add_f32_e32 v107, v43, v107
	v_cvt_pk_bf16_f32 v111, v44, v45
	v_add_f32_e32 v106, v44, v106
	v_add_f32_e32 v107, v45, v107
	v_cvt_pk_bf16_f32 v108, v38, v39
	v_add_f32_e32 v106, v46, v106
	v_add_f32_e32 v107, v47, v107
	v_cvt_pk_bf16_f32 v112, v46, v47
	v_add_f32_e32 v106, v48, v106
	v_add_f32_e32 v107, v49, v107
	v_cvt_pk_bf16_f32 v109, v40, v41
	v_add_f32_e32 v117, v106, v107
	v_cvt_pk_bf16_f32 v106, v34, v35
	v_cvt_pk_bf16_f32 v107, v36, v37
	v_cvt_pk_bf16_f32 v113, v48, v49
	s_waitcnt lgkmcnt(8)
	s_nop 0
	v_mfma_f32_32x32x16_bf16 v[2:17], v[50:53], v[58:61], v[2:17]
	v_mfma_f32_32x32x16_bf16 v[2:17], v[54:57], v[62:65], v[2:17]
	v_mfma_f32_32x32x16_bf16 v[2:17], v[106:109], v[82:85], v[2:17]
	v_mfma_f32_32x32x16_bf16 v[2:17], v[110:113], v[86:89], v[2:17]
	s_waitcnt lgkmcnt(0)
	v_add_f32_e32 v139, v139, v117
	v_mfma_f32_32x32x16_bf16 v[18:33], v[50:53], v[90:93], v[18:33]
	v_mfma_f32_32x32x16_bf16 v[18:33], v[54:57], v[94:97], v[18:33]
	v_mfma_f32_32x32x16_bf16 v[18:33], v[106:109], v[98:101], v[18:33]
	v_mfma_f32_32x32x16_bf16 v[18:33], v[110:113], v[102:105], v[18:33]
	s_mov_b64 s[4:5], -1
	s_and_b64 vcc, exec, s[12:13]
	s_cbranch_vccnz .LBB0_305

; __device__ __forceinline__ unsigned cvtpk(float lo, float hi) { f32x2_t v = {lo, hi}; bf16x2_t b = __builtin_convertvector(v, bf16x2_t); return __builtin_bit_cast(unsigned, b); }
; template <class BIAS>
; __device__ __forceinline__ void attn_tiles(char* shm, const UnitIO& io, int t_begin, int t_end, const BIAS& B, int tid) {
;     ...
;             for (int d0 = 0; d0 < 4; ++d0) { c0 = __builtin_amdgcn_mfma_f32_32x32x16_bf16(kf[2 * d0], qr[d0], c0, 0, 0, 0); c1 = __builtin_amdgcn_mfma_f32_32x32x16_bf16(kf[2 * d0 + 1], qr[d0], c1, 0, 0, 0); }
;             float s0 = 0.f;
; #pragma unroll
;             for (int r = 0; r < 16; ++r) c0[r] = __builtin_amdgcn_exp2f(c0[r]);
;             { f32x2_t s2 = (f32x2_t){c0[0], c0[1]};
; #pragma unroll
;               for (int i = 1; i < 8; ++i) s2 += (f32x2_t){c0[2 * i], c0[2 * i + 1]};
;               s0 = s2[0] + s2[1]; }
;             l_reg += s0;
; #pragma unroll
;             for (int i = 0; i < 4; ++i) { pw[0][i] = cvtpk(c0[2 * i], c0[2 * i + 1]); pw[1][i] = cvtpk(c0[8 + 2 * i], c0[9 + 2 * i]); }
;             c1x = c1;
.LBB0_347:
	s_nop 1
	v_mfma_f32_32x32x16_bf16 v[66:81], v[114:117], v[82:85], v[66:81]
	v_mfma_f32_32x32x16_bf16 v[66:81], v[118:121], v[86:89], v[66:81]
	v_mfma_f32_32x32x16_bf16 v[50:65], v[110:113], v[82:85], v[50:65]
	v_mfma_f32_32x32x16_bf16 v[66:81], v[122:125], v[90:93], v[66:81]
	v_mfma_f32_32x32x16_bf16 v[50:65], v[106:109], v[86:89], v[50:65]
	v_mfma_f32_32x32x16_bf16 v[66:81], v[126:129], v[94:97], v[66:81]
	v_mfma_f32_32x32x16_bf16 v[50:65], v[102:105], v[90:93], v[50:65]
	s_nop 10
	v_exp_f32_e32 v66, v66
	v_exp_f32_e32 v67, v67
	v_exp_f32_e32 v68, v68
	v_exp_f32_e32 v69, v69
	v_exp_f32_e32 v114, v70
	v_exp_f32_e32 v115, v71
	v_exp_f32_e32 v116, v72
	v_exp_f32_e32 v117, v73
	v_exp_f32_e32 v70, v74
	v_exp_f32_e32 v71, v75
	v_exp_f32_e32 v72, v76
	v_exp_f32_e32 v73, v77
	v_exp_f32_e32 v74, v78
	v_exp_f32_e32 v75, v79
	v_add_f32_e32 v78, v66, v68
	v_add_f32_e32 v79, v67, v69
	v_mfma_f32_32x32x16_bf16 v[50:65], v[98:101], v[94:97], v[50:65]
	v_add_f32_e64 v78, v114, v78
	v_add_f32_e64 v79, v115, v79
	v_exp_f32_e32 v76, v80
	v_exp_f32_e32 v77, v81
	v_add_f32_e32 v78, v116, v78
	v_add_f32_e32 v79, v117, v79
	v_cvt_pk_bf16_f32 v66, v66, v67
	v_add_f32_e32 v78, v70, v78
	v_add_f32_e32 v79, v71, v79
	v_cvt_pk_bf16_f32 v70, v70, v71
	v_add_f32_e32 v78, v72, v78
	v_add_f32_e32 v79, v73, v79
	v_cvt_pk_bf16_f32 v67, v68, v69
	v_add_f32_e32 v78, v74, v78
	v_add_f32_e32 v79, v75, v79
	v_cvt_pk_bf16_f32 v71, v72, v73
	v_add_f32_e32 v78, v76, v78
	v_add_f32_e32 v79, v77, v79
	v_cvt_pk_bf16_f32 v68, v114, v115
	v_add_f32_e32 v78, v78, v79
	v_cvt_pk_bf16_f32 v72, v74, v75
	v_cvt_pk_bf16_f32 v69, v116, v117
	v_cvt_pk_bf16_f32 v73, v76, v77
	v_add_f32_e32 v135, v135, v78
	s_and_b64 vcc, exec, s[34:35]
	s_cbranch_vccz .LBB0_355

; __device__ __forceinline__ unsigned cvtpk(float lo, float hi) { f32x2_t v = {lo, hi}; bf16x2_t b = __builtin_convertvector(v, bf16x2_t); return __builtin_bit_cast(unsigned, b); }
; __device__ __forceinline__ s16x4 vtr(lds_cptr p) { return __builtin_bit_cast(s16x4, __builtin_amdgcn_ds_read_tr16_b64_v4i16((__attribute__((address_space(3))) v4i16_t*)p)); }
; template <class BIAS>
; __device__ __forceinline__ void attn_tiles(char* shm, const UnitIO& io, int t_begin, int t_end, const BIAS& B, int tid) {
;     ...
;         if (act) {
;             const lds_cptr vp = vp0 + sl_c;
;             s16x4 vlo[8], vhi[8];
; #pragma unroll
;             for (int i = 0; i < 8; ++i) { vlo[i] = vtr(vp + (i >> 2) * 4096 + (i & 3) * 1024); vhi[i] = vtr(vp + (i >> 2) * 4096 + (i & 3) * 1024 + 512); }
;             ATT_SBAR();
;             { float s1 = 0.f;
; #pragma unroll
;               for (int r = 0; r < 16; ++r) c1x[r] = __builtin_amdgcn_exp2f(c1x[r]);
;               { f32x2_t s2 = (f32x2_t){c1x[0], c1x[1]};
; #pragma unroll
;                 for (int i = 1; i < 8; ++i) s2 += (f32x2_t){c1x[2 * i], c1x[2 * i + 1]};
;                 s1 = s2[0] + s2[1]; }
;               l_reg += s1;
; #pragma unroll
;               for (int i = 0; i < 4; ++i) { pw[2][i] = cvtpk(c1x[2 * i], c1x[2 * i + 1]); pw[3][i] = cvtpk(c1x[8 + 2 * i], c1x[9 + 2 * i]); } }
;             ATT_SBAR();
;             asm volatile("" : "+v"(vlo[0]), "+v"(vhi[0]), "+v"(vlo[1]), "+v"(vhi[1]), "+v"(vlo[2]), "+v"(vhi[2]), "+v"(vlo[3]), "+v"(vhi[3]));
; #pragma unroll
;             for (int ks = 0; ks < 4; ++ks) { const bf16x8 vf = (bf16x8){vlo[ks][0], vlo[ks][1], vlo[ks][2], vlo[ks][3], vhi[ks][0], vhi[ks][1], vhi[ks][2], vhi[ks][3]};
;                 o[0] = __builtin_amdgcn_mfma_f32_32x32x16_bf16(__builtin_bit_cast(bf16x8, pw[ks]), vf, o[0], 0, 0, 0); }
;             ATT_SBAR();
;             asm volatile("" : "+v"(vlo[4]), "+v"(vhi[4]), "+v"(vlo[5]), "+v"(vhi[5]), "+v"(vlo[6]), "+v"(vhi[6]), "+v"(vlo[7]), "+v"(vhi[7]));
; #pragma unroll
;             for (int ks = 0; ks < 4; ++ks) { const bf16x8 vf = (bf16x8){vlo[4 + ks][0], vlo[4 + ks][1], vlo[4 + ks][2], vlo[4 + ks][3], vhi[4 + ks][0], vhi[4 + ks][1], vhi[4 + ks][2], vhi[4 + ks][3]};
;                 o[1] = __builtin_amdgcn_mfma_f32_32x32x16_bf16(__builtin_bit_cast(bf16x8, pw[ks]), vf, o[1], 0, 0, 0); }
;         }
.LBB0_355:
	v_add_u32_e32 v120, s20, v180
	ds_read_b64_tr_b16 v[74:75], v120 offset:32768
	ds_read_b64_tr_b16 v[76:77], v120 offset:33280
	ds_read_b64_tr_b16 v[78:79], v120 offset:33792
	ds_read_b64_tr_b16 v[80:81], v120 offset:34304
	ds_read_b64_tr_b16 v[98:99], v120 offset:34816
	ds_read_b64_tr_b16 v[100:101], v120 offset:35328
	ds_read_b64_tr_b16 v[102:103], v120 offset:35840
	ds_read_b64_tr_b16 v[104:105], v120 offset:36352
	ds_read_b64_tr_b16 v[106:107], v120 offset:36864
	ds_read_b64_tr_b16 v[108:109], v120 offset:37376
	ds_read_b64_tr_b16 v[110:111], v120 offset:37888
	ds_read_b64_tr_b16 v[112:113], v120 offset:38400
	ds_read_b64_tr_b16 v[114:115], v120 offset:38912
	ds_read_b64_tr_b16 v[116:117], v120 offset:39424
	ds_read_b64_tr_b16 v[118:119], v120 offset:39936
	ds_read_b64_tr_b16 v[120:121], v120 offset:40448
	v_exp_f32_e32 v50, v50
	v_exp_f32_e32 v51, v51
	v_exp_f32_e32 v52, v52
	v_exp_f32_e32 v53, v53
	v_exp_f32_e32 v54, v54
	v_exp_f32_e32 v55, v55
	v_exp_f32_e32 v56, v56
	v_exp_f32_e32 v57, v57
	v_exp_f32_e32 v58, v58
	v_exp_f32_e32 v59, v59
	v_exp_f32_e32 v60, v60
	v_exp_f32_e32 v61, v61
	v_add_f32_e32 v122, v52, v50
	v_add_f32_e32 v123, v53, v51
	v_exp_f32_e32 v62, v62
	v_exp_f32_e32 v63, v63
	v_add_f32_e32 v122, v54, v122
	v_add_f32_e32 v123, v55, v123
	v_exp_f32_e32 v64, v64
	v_exp_f32_e32 v65, v65
	v_add_f32_e32 v122, v56, v122
	v_add_f32_e32 v123, v57, v123
	v_cvt_pk_bf16_f32 v126, v58, v59
	v_add_f32_e32 v122, v58, v122
	v_add_f32_e32 v123, v59, v123
	v_cvt_pk_bf16_f32 v127, v60, v61
	v_add_f32_e32 v122, v60, v122
	v_add_f32_e32 v123, v61, v123
	v_cvt_pk_bf16_f32 v124, v54, v55
	v_add_f32_e32 v122, v62, v122
	v_add_f32_e32 v123, v63, v123
	v_cvt_pk_bf16_f32 v128, v62, v63
	v_add_f32_e32 v122, v64, v122
	v_add_f32_e32 v123, v65, v123
	v_cvt_pk_bf16_f32 v125, v56, v57
	v_add_f32_e32 v139, v122, v123
	v_cvt_pk_bf16_f32 v122, v50, v51
	v_cvt_pk_bf16_f32 v123, v52, v53
	v_cvt_pk_bf16_f32 v129, v64, v65
	s_waitcnt lgkmcnt(8)
	s_nop 0
	v_mfma_f32_32x32x16_bf16 v[12:27], v[66:69], v[74:77], v[12:27]
	v_mfma_f32_32x32x16_bf16 v[12:27], v[70:73], v[78:81], v[12:27]
	v_mfma_f32_32x32x16_bf16 v[12:27], v[122:125], v[98:101], v[12:27]
	v_mfma_f32_32x32x16_bf16 v[12:27], v[126:129], v[102:105], v[12:27]
	s_waitcnt lgkmcnt(0)
	v_add_f32_e32 v135, v135, v139
	v_mfma_f32_32x32x16_bf16 v[34:49], v[66:69], v[106:109], v[34:49]
	s_nop 8
	v_mov_b32_e32 v202, v12
	v_mov_b32_e32 v200, v13
	v_mov_b32_e32 v198, v14
	v_mov_b32_e32 v196, v15
	v_mov_b32_e32 v176, v16
	v_mov_b32_e32 v174, v17
	v_mov_b32_e32 v172, v18
	v_mfma_f32_32x32x16_bf16 v[34:49], v[70:73], v[110:113], v[34:49]
	v_mov_b32_e32 v170, v19
	v_mov_b32_e32 v169, v20
	v_mov_b32_e32 v167, v21
	v_mov_b32_e32 v153, v22
	v_mov_b32_e32 v149, v23
	v_mov_b32_e32 v168, v24
	v_mov_b32_e32 v166, v25
	v_mfma_f32_32x32x16_bf16 v[34:49], v[122:125], v[114:117], v[34:49]
	v_mov_b32_e32 v151, v26
	v_mov_b32_e32 v139, v27
	v_mfma_f32_32x32x16_bf16 v[34:49], v[126:129], v[118:121], v[34:49]
	s_nop 11
	v_mov_b32_e32 v211, v34
	v_mov_b32_e32 v210, v35
	v_mov_b32_e32 v209, v36
	v_mov_b32_e32 v208, v37
	v_mov_b32_e32 v207, v38
	v_mov_b32_e32 v206, v39
	v_mov_b32_e32 v205, v40
	v_mov_b32_e32 v204, v41
	v_mov_b32_e32 v203, v42
	v_mov_b32_e32 v201, v43
	v_mov_b32_e32 v199, v44
	v_mov_b32_e32 v197, v45
	v_mov_b32_e32 v177, v46
	v_mov_b32_e32 v175, v47
	v_mov_b32_e32 v173, v48
	v_mov_b32_e32 v171, v49
	s_mov_b64 s[34:35], -1
	s_and_b64 vcc, exec, s[46:47]
	s_cbranch_vccnz .LBB0_349

;     __device__ __forceinline__ void init(f32x16& c0, f32x16& c1, int t) const {
;         const int dt = t - (w >> 1);
;         const float base = basel + (float)dt * d64;
; #pragma unroll
;         for (int i = 0; i < 8; ++i) { const f32x2_t p = kc[i] + base, q = p + d32; c0[2 * i] = p[0]; c0[2 * i + 1] = p[1]; c1[2 * i] = q[0]; c1[2 * i + 1] = q[1]; }
;         if (dt == 0) {
; #pragma unroll
;             for (int r = 0; r < 16; ++r) { const int ko = (r & 3) + 8 * (r >> 2); if (ko < u) c0[r] = ATT_NEG; if (ko < u - 32) c1[r] = ATT_NEG; }
;         } else if (dt == 2) {
; #pragma unroll
;             for (int r = 0; r < 16; ++r) { const int ko = (r & 3) + 8 * (r >> 2); if (ko > u) c0[r] = ATT_NEG; if (ko > u - 32) c1[r] = ATT_NEG; }
;         }
;     }
.LBB0_367:
	s_cmp_ge_i32 s88, s73
	s_cselect_b64 s[56:57], -1, 0
	s_cmp_le_i32 s88, s33
	s_cselect_b64 s[70:71], -1, 0
	s_and_b64 s[70:71], s[56:57], s[70:71]
	s_add_i32 s56, s81, 0xffffa000
	v_cndmask_b32_e64 v58, 0, 1, s[70:71]
	s_and_b32 s82, s56, 0x6000
	v_cmp_ne_u32_e64 s[56:57], 1, v58
	s_andn2_b64 vcc, exec, s[70:71]
	s_cbranch_vccnz .LBB0_374
	v_add_u32_e32 v34, s82, v181
	ds_read_b128 v[130:133], v34
	ds_read_b128 v[126:129], v34 offset:512
	ds_read_b128 v[134:137], v34 offset:2048
	ds_read_b128 v[122:125], v34 offset:2560
	ds_read_b128 v[138:141], v34 offset:4096
	ds_read_b128 v[118:121], v34 offset:4608
	ds_read_b128 v[142:145], v34 offset:6144
	ds_read_b128 v[114:117], v34 offset:6656
	s_add_u32 s70, s72, s88
	v_cvt_f32_i32_e32 v34, s70
	v_mov_b32_e32 v157, v156
	s_cmp_lg_u32 s70, 0
	v_fma_f32 v34, v149, v34, -v0
	v_add_f32_e32 v50, v154, v34
	v_add_f32_e32 v51, v155, v34
	v_add_f32_e32 v52, v158, v34
	v_add_f32_e32 v53, v159, v34
	v_add_f32_e32 v54, v160, v34
	v_add_f32_e32 v55, v161, v34
	v_add_f32_e32 v56, v162, v34
	v_add_f32_e32 v57, v163, v34
	v_add_f32_e32 v58, v164, v34
	v_add_f32_e32 v59, v165, v34
	v_add_f32_e32 v60, v166, v34
	v_add_f32_e32 v61, v167, v34
	v_add_f32_e32 v62, v168, v34
	v_add_f32_e32 v63, v169, v34
	v_add_f32_e32 v64, v170, v34
	v_add_f32_e32 v65, v171, v34
	v_add_f32_e32 v78, v156, v62
	v_add_f32_e32 v79, v157, v63
	v_add_f32_e32 v80, v156, v64
	v_add_f32_e32 v81, v157, v65
	v_add_f32_e32 v76, v156, v60
	v_add_f32_e32 v77, v157, v61
	v_add_f32_e32 v74, v156, v58
	v_add_f32_e32 v75, v157, v59
	v_add_f32_e32 v72, v156, v56
	v_add_f32_e32 v73, v157, v57
	v_add_f32_e32 v70, v156, v54
	v_add_f32_e32 v71, v157, v55
	v_add_f32_e32 v68, v156, v52
	v_add_f32_e32 v69, v157, v53
	v_add_f32_e32 v66, v176, v50
	v_add_f32_e32 v67, v177, v51
	s_cbranch_scc0 .LBB0_377
	v_mov_b64_e32 v[96:97], v[64:65]
	v_mov_b64_e32 v[34:35], v[66:67]
	s_mov_b64 vcc, 0
	s_cmp_eq_u32 s70, 2
	s_mov_b64 s[70:71], 0
	v_mov_b64_e32 v[94:95], v[62:63]
	v_mov_b64_e32 v[92:93], v[60:61]
	v_mov_b64_e32 v[90:91], v[58:59]
	v_mov_b64_e32 v[88:89], v[56:57]
	v_mov_b64_e32 v[86:87], v[54:55]
	v_mov_b64_e32 v[84:85], v[52:53]
	v_mov_b64_e32 v[82:83], v[50:51]
	v_mov_b64_e32 v[36:37], v[68:69]
	v_mov_b64_e32 v[38:39], v[70:71]
	v_mov_b64_e32 v[40:41], v[72:73]
	v_mov_b64_e32 v[42:43], v[74:75]
	v_mov_b64_e32 v[44:45], v[76:77]
	v_mov_b64_e32 v[46:47], v[78:79]
	v_mov_b64_e32 v[48:49], v[80:81]
	s_cbranch_scc1 .LBB0_388
	s_and_b64 vcc, exec, vcc
	s_cbranch_vccz .LBB0_378

; __device__ __forceinline__ unsigned cvtpk(float lo, float hi) { f32x2_t v = {lo, hi}; bf16x2_t b = __builtin_convertvector(v, bf16x2_t); return __builtin_bit_cast(unsigned, b); }
; __device__ __forceinline__ s16x4 vtr(lds_cptr p) { return __builtin_bit_cast(s16x4, __builtin_amdgcn_ds_read_tr16_b64_v4i16((__attribute__((address_space(3))) v4i16_t*)p)); }
; template <class BIAS>
; __device__ __forceinline__ void attn_tiles(char* shm, const UnitIO& io, int t_begin, int t_end, const BIAS& B, int tid) {
;     ...
;         if (act) {
;             const lds_cptr vp = vp0 + sl_c;
;             s16x4 vlo[8], vhi[8];
; #pragma unroll
;             for (int i = 0; i < 8; ++i) { vlo[i] = vtr(vp + (i >> 2) * 4096 + (i & 3) * 1024); vhi[i] = vtr(vp + (i >> 2) * 4096 + (i & 3) * 1024 + 512); }
;             ATT_SBAR();
;             { float s1 = 0.f;
; #pragma unroll
;               for (int r = 0; r < 16; ++r) c1x[r] = __builtin_amdgcn_exp2f(c1x[r]);
;               { f32x2_t s2 = (f32x2_t){c1x[0], c1x[1]};
; #pragma unroll
;                 for (int i = 1; i < 8; ++i) s2 += (f32x2_t){c1x[2 * i], c1x[2 * i + 1]};
;                 s1 = s2[0] + s2[1]; }
;               l_reg += s1;
; #pragma unroll
;               for (int i = 0; i < 4; ++i) { pw[2][i] = cvtpk(c1x[2 * i], c1x[2 * i + 1]); pw[3][i] = cvtpk(c1x[8 + 2 * i], c1x[9 + 2 * i]); } }
;             ATT_SBAR();
;             asm volatile("" : "+v"(vlo[0]), "+v"(vhi[0]), "+v"(vlo[1]), "+v"(vhi[1]), "+v"(vlo[2]), "+v"(vhi[2]), "+v"(vlo[3]), "+v"(vhi[3]));
; #pragma unroll
;             for (int ks = 0; ks < 4; ++ks) { const bf16x8 vf = (bf16x8){vlo[ks][0], vlo[ks][1], vlo[ks][2], vlo[ks][3], vhi[ks][0], vhi[ks][1], vhi[ks][2], vhi[ks][3]};
;                 o[0] = __builtin_amdgcn_mfma_f32_32x32x16_bf16(__builtin_bit_cast(bf16x8, pw[ks]), vf, o[0], 0, 0, 0); }
;             ATT_SBAR();
;             asm volatile("" : "+v"(vlo[4]), "+v"(vhi[4]), "+v"(vlo[5]), "+v"(vhi[5]), "+v"(vlo[6]), "+v"(vhi[6]), "+v"(vlo[7]), "+v"(vhi[7]));
; #pragma unroll
;             for (int ks = 0; ks < 4; ++ks) { const bf16x8 vf = (bf16x8){vlo[4 + ks][0], vlo[4 + ks][1], vlo[4 + ks][2], vlo[4 + ks][3], vhi[4 + ks][0], vhi[4 + ks][1], vhi[4 + ks][2], vhi[4 + ks][3]};
;                 o[1] = __builtin_amdgcn_mfma_f32_32x32x16_bf16(__builtin_bit_cast(bf16x8, pw[ks]), vf, o[1], 0, 0, 0); }
;         }
.LBB0_375:
	v_add_u32_e32 v88, s82, v180
	ds_read_b64_tr_b16 v[58:59], v88 offset:32768
	ds_read_b64_tr_b16 v[60:61], v88 offset:33280
	ds_read_b64_tr_b16 v[62:63], v88 offset:33792
	ds_read_b64_tr_b16 v[64:65], v88 offset:34304
	ds_read_b64_tr_b16 v[66:67], v88 offset:34816
	ds_read_b64_tr_b16 v[68:69], v88 offset:35328
	ds_read_b64_tr_b16 v[70:71], v88 offset:35840
	ds_read_b64_tr_b16 v[72:73], v88 offset:36352
	ds_read_b64_tr_b16 v[74:75], v88 offset:36864
	ds_read_b64_tr_b16 v[76:77], v88 offset:37376
	ds_read_b64_tr_b16 v[78:79], v88 offset:37888
	ds_read_b64_tr_b16 v[80:81], v88 offset:38400
	ds_read_b64_tr_b16 v[82:83], v88 offset:38912
	ds_read_b64_tr_b16 v[84:85], v88 offset:39424
	ds_read_b64_tr_b16 v[86:87], v88 offset:39936
	ds_read_b64_tr_b16 v[88:89], v88 offset:40448
	v_exp_f32_e32 v34, v34
	v_exp_f32_e32 v35, v35
	v_exp_f32_e32 v36, v36
	v_exp_f32_e32 v37, v37
	v_exp_f32_e32 v38, v38
	v_exp_f32_e32 v39, v39
	v_exp_f32_e32 v40, v40
	v_exp_f32_e32 v41, v41
	v_exp_f32_e32 v42, v42
	v_exp_f32_e32 v43, v43
	v_exp_f32_e32 v44, v44
	v_exp_f32_e32 v45, v45
	v_add_f32_e32 v90, v36, v34
	v_add_f32_e32 v91, v37, v35
	v_exp_f32_e32 v46, v46
	v_exp_f32_e32 v47, v47
	v_add_f32_e32 v90, v38, v90
	v_add_f32_e32 v91, v39, v91
	v_exp_f32_e32 v48, v48
	v_exp_f32_e32 v49, v49
	v_add_f32_e32 v90, v40, v90
	v_add_f32_e32 v91, v41, v91
	v_cvt_pk_bf16_f32 v94, v42, v43
	v_add_f32_e32 v90, v42, v90
	v_add_f32_e32 v91, v43, v91
	v_cvt_pk_bf16_f32 v95, v44, v45
	v_add_f32_e32 v90, v44, v90
	v_add_f32_e32 v91, v45, v91
	v_cvt_pk_bf16_f32 v92, v38, v39
	v_add_f32_e32 v90, v46, v90
	v_add_f32_e32 v91, v47, v91
	v_cvt_pk_bf16_f32 v96, v46, v47
	v_add_f32_e32 v90, v48, v90
	v_add_f32_e32 v91, v49, v91
	v_cvt_pk_bf16_f32 v93, v40, v41
	v_add_f32_e32 v114, v90, v91
	v_cvt_pk_bf16_f32 v90, v34, v35
	v_cvt_pk_bf16_f32 v91, v36, v37
	v_cvt_pk_bf16_f32 v97, v48, v49
	s_waitcnt lgkmcnt(8)
	s_nop 0
	v_mfma_f32_32x32x16_bf16 v[2:17], v[50:53], v[58:61], v[2:17]
	v_mfma_f32_32x32x16_bf16 v[2:17], v[54:57], v[62:65], v[2:17]
	v_mfma_f32_32x32x16_bf16 v[2:17], v[90:93], v[66:69], v[2:17]
	v_mfma_f32_32x32x16_bf16 v[2:17], v[94:97], v[70:73], v[2:17]
	s_waitcnt lgkmcnt(0)
	v_add_f32_e32 v151, v151, v114
	v_mfma_f32_32x32x16_bf16 v[18:33], v[50:53], v[74:77], v[18:33]
	v_mfma_f32_32x32x16_bf16 v[18:33], v[54:57], v[78:81], v[18:33]
	v_mfma_f32_32x32x16_bf16 v[18:33], v[90:93], v[82:85], v[18:33]
	v_mfma_f32_32x32x16_bf16 v[18:33], v[94:97], v[86:89], v[18:33]
	s_mov_b64 s[56:57], -1
	s_and_b64 vcc, exec, s[68:69]
	s_cbranch_vccnz .LBB0_382

; __device__ __forceinline__ unsigned cvtpk(float lo, float hi) { f32x2_t v = {lo, hi}; bf16x2_t b = __builtin_convertvector(v, bf16x2_t); return __builtin_bit_cast(unsigned, b); }
; template <class BIAS>
; __device__ __forceinline__ void attn_tiles(char* shm, const UnitIO& io, int t_begin, int t_end, const BIAS& B, int tid) {
;     ...
;             for (int d0 = 0; d0 < 4; ++d0) { c0 = __builtin_amdgcn_mfma_f32_32x32x16_bf16(kf[2 * d0], qr[d0], c0, 0, 0, 0); c1 = __builtin_amdgcn_mfma_f32_32x32x16_bf16(kf[2 * d0 + 1], qr[d0], c1, 0, 0, 0); }
;             float s0 = 0.f;
; #pragma unroll
;             for (int r = 0; r < 16; ++r) c0[r] = __builtin_amdgcn_exp2f(c0[r]);
;             { f32x2_t s2 = (f32x2_t){c0[0], c0[1]};
; #pragma unroll
;               for (int i = 1; i < 8; ++i) s2 += (f32x2_t){c0[2 * i], c0[2 * i + 1]};
;               s0 = s2[0] + s2[1]; }
;             l_reg += s0;
; #pragma unroll
;             for (int i = 0; i < 4; ++i) { pw[0][i] = cvtpk(c0[2 * i], c0[2 * i + 1]); pw[1][i] = cvtpk(c0[8 + 2 * i], c0[9 + 2 * i]); }
;             c1x = c1;
.LBB0_380:
	s_or_b64 exec, exec, vcc
	s_waitcnt lgkmcnt(0)
	s_nop 0
	v_mfma_f32_32x32x16_bf16 v[82:97], v[130:133], v[98:101], v[82:97]
	v_mfma_f32_32x32x16_bf16 v[82:97], v[134:137], v[102:105], v[82:97]
	v_mfma_f32_32x32x16_bf16 v[34:49], v[126:129], v[98:101], v[34:49]
	v_mfma_f32_32x32x16_bf16 v[82:97], v[138:141], v[106:109], v[82:97]
	v_mfma_f32_32x32x16_bf16 v[34:49], v[122:125], v[102:105], v[34:49]
	v_mfma_f32_32x32x16_bf16 v[82:97], v[142:145], v[110:113], v[82:97]
	v_mfma_f32_32x32x16_bf16 v[34:49], v[118:121], v[106:109], v[34:49]
	s_nop 10
	v_exp_f32_e32 v50, v82
	v_exp_f32_e32 v51, v83
	v_exp_f32_e32 v52, v84
	v_exp_f32_e32 v53, v85
	v_exp_f32_e32 v56, v86
	v_exp_f32_e32 v57, v87
	v_exp_f32_e32 v58, v88
	v_exp_f32_e32 v59, v89
	v_exp_f32_e32 v54, v90
	v_exp_f32_e32 v55, v91
	v_exp_f32_e32 v60, v92
	v_exp_f32_e32 v61, v93
	v_add_f32_e32 v66, v50, v52
	v_add_f32_e32 v67, v51, v53
	v_exp_f32_e32 v62, v94
	v_exp_f32_e32 v63, v95
	v_add_f32_e32 v66, v56, v66
	v_add_f32_e32 v67, v57, v67
	v_mfma_f32_32x32x16_bf16 v[34:49], v[114:117], v[110:113], v[34:49]
	v_exp_f32_e32 v64, v96
	v_exp_f32_e32 v65, v97
	v_add_f32_e32 v66, v58, v66
	v_add_f32_e32 v67, v59, v67
	v_cvt_pk_bf16_f32 v50, v50, v51
	v_add_f32_e32 v66, v54, v66
	v_add_f32_e32 v67, v55, v67
	v_cvt_pk_bf16_f32 v54, v54, v55
	v_add_f32_e32 v66, v60, v66
	v_add_f32_e32 v67, v61, v67
	v_cvt_pk_bf16_f32 v51, v52, v53
	v_add_f32_e32 v66, v62, v66
	v_add_f32_e32 v67, v63, v67
	v_cvt_pk_bf16_f32 v55, v60, v61
	v_add_f32_e32 v66, v64, v66
	v_add_f32_e32 v67, v65, v67
	v_cvt_pk_bf16_f32 v52, v56, v57
	v_add_f32_e32 v66, v66, v67
	v_cvt_pk_bf16_f32 v56, v62, v63
	v_cvt_pk_bf16_f32 v53, v58, v59
	v_cvt_pk_bf16_f32 v57, v64, v65
	v_add_f32_e32 v151, v151, v66
	s_and_b64 vcc, exec, s[56:57]
	s_cbranch_vccz .LBB0_375
